# layer-1 QKV epilogue row-norm: xor-32 reduction step via v_permlane32_swap instead of ds_bpermute (on top of the peeled out-projection GEMMs)
# speedup vs baseline: 1.0046x; 1.0046x over previous
;     __device__ __forceinline__ void operator()(const f32x4 (&acc)[2][2][4][2], const Unit& u, int wr, int wc, int fr, int fq) const {
;     ...
;                 for (int m = 0; m < 4; ++m) { float s_ = 0.f;
; #pragma unroll
;                     for (int q = 0; q < 4; ++q) { const f32x4 v = acc[ai][q >> 1][m][q & 1]; s_ += v[0] * v[0] + v[1] * v[1] + v[2] * v[2] + v[3] * v[3]; }
;                     s_ += __shfl_xor(s_, 16); s_ += __shfl_xor(s_, 32);
;                     if (fq == 0) xb[(ai * HALF + m * 16) * 4 + wc] = s_; }
.LBB0_1024:
	v_mov_b32_e32 v2, v1
	s_nop 15
	s_nop 7
	s_cmp_lt_i32 s66, 16
	v_add_u32_e32 v2, s54, v2
	s_cselect_b64 s[22:23], -1, 0
	s_cmp_gt_i32 s66, 15
	v_lshl_add_u32 v18, v2, 4, s60
	s_cbranch_scc1 .LBB0_1042
	v_mul_f32_e32 v4, v191, v191
	v_mul_f32_e32 v5, v187, v187
	v_fmac_f32_e32 v4, v190, v190
	v_fmac_f32_e32 v5, v186, v186
	v_fmac_f32_e32 v4, v192, v192
	v_fmac_f32_e32 v5, v188, v188
	v_fmac_f32_e32 v4, v193, v193
	v_fmac_f32_e32 v5, v189, v189
	v_add_f32_e32 v4, v4, v5
	v_mul_f32_e32 v5, v183, v183
	v_fmac_f32_e32 v5, v182, v182
	v_fmac_f32_e32 v5, v184, v184
	v_fmac_f32_e32 v5, v185, v185
	v_and_b32_e32 v3, 64, v250
	v_add_f32_e32 v4, v4, v5
	v_mul_f32_e32 v5, v179, v179
	v_xor_b32_e32 v2, 16, v250
	v_add_u32_e32 v3, 64, v3
	v_fmac_f32_e32 v5, v178, v178
	v_cmp_lt_i32_e32 vcc, v2, v3
	v_fmac_f32_e32 v5, v180, v180
	v_fmac_f32_e32 v5, v181, v181
	v_cndmask_b32_e32 v2, v250, v2, vcc
	v_lshlrev_b32_e32 v2, 2, v2
	v_add_f32_e32 v5, v4, v5
	ds_bpermute_b32 v6, v2, v5
	v_xor_b32_e32 v4, 32, v250
	v_cmp_lt_i32_e32 vcc, v4, v3
	s_waitcnt lgkmcnt(0)
	v_add_f32_e32 v5, v5, v6
	v_cndmask_b32_e32 v3, v250, v4, vcc
	v_lshlrev_b32_e32 v4, 2, v3
	v_mov_b32_e32 v6, v5
	s_nop 1
	v_permlane32_swap_b32_e32 v6, v5
	v_lshl_add_u32 v3, s52, 2, v18
	s_and_saveexec_b64 s[8:9], s[0:1]
	s_cbranch_execz .LBB0_1027
	s_waitcnt lgkmcnt(0)
	v_add_f32_e32 v5, v5, v6
	ds_write_b32 v3, v5
.LBB0_1027:
	s_or_b64 exec, exec, s[8:9]
	v_mul_f32_e32 v5, v175, v175
	s_waitcnt lgkmcnt(0)
	v_mul_f32_e32 v6, v171, v171
	v_fmac_f32_e32 v5, v174, v174
	v_fmac_f32_e32 v6, v170, v170
	v_fmac_f32_e32 v5, v176, v176
	v_fmac_f32_e32 v6, v172, v172
	v_fmac_f32_e32 v5, v177, v177
	v_fmac_f32_e32 v6, v173, v173
	v_add_f32_e32 v5, v5, v6
	v_mul_f32_e32 v6, v167, v167
	v_fmac_f32_e32 v6, v166, v166
	v_fmac_f32_e32 v6, v168, v168
	v_fmac_f32_e32 v6, v169, v169
	v_add_f32_e32 v5, v5, v6
	v_mul_f32_e32 v6, v163, v163
	v_fmac_f32_e32 v6, v162, v162
	v_fmac_f32_e32 v6, v164, v164
	v_fmac_f32_e32 v6, v165, v165
	v_add_f32_e32 v5, v5, v6
	ds_bpermute_b32 v6, v2, v5
	s_waitcnt lgkmcnt(0)
	v_add_f32_e32 v5, v5, v6
	v_mov_b32_e32 v6, v5
	s_nop 1
	v_permlane32_swap_b32_e32 v6, v5
	s_and_saveexec_b64 s[8:9], s[0:1]
	s_cbranch_execz .LBB0_1029
	s_waitcnt lgkmcnt(0)
	v_add_f32_e32 v5, v5, v6
	ds_write_b32 v3, v5 offset:256
.LBB0_1029:
	s_or_b64 exec, exec, s[8:9]
	v_mul_f32_e32 v5, v159, v159
	s_waitcnt lgkmcnt(0)
	v_mul_f32_e32 v6, v155, v155
	v_fmac_f32_e32 v5, v158, v158
	v_fmac_f32_e32 v6, v154, v154
	v_fmac_f32_e32 v5, v160, v160
	v_fmac_f32_e32 v6, v156, v156
	v_fmac_f32_e32 v5, v161, v161
	v_fmac_f32_e32 v6, v157, v157
	v_add_f32_e32 v5, v5, v6
	v_mul_f32_e32 v6, v151, v151
	v_fmac_f32_e32 v6, v150, v150
	v_fmac_f32_e32 v6, v152, v152
	v_fmac_f32_e32 v6, v153, v153
	v_add_f32_e32 v5, v5, v6
	v_mul_f32_e32 v6, v147, v147
	v_fmac_f32_e32 v6, v146, v146
	v_fmac_f32_e32 v6, v148, v148
	v_fmac_f32_e32 v6, v149, v149
	v_add_f32_e32 v5, v5, v6
	ds_bpermute_b32 v6, v2, v5
	s_waitcnt lgkmcnt(0)
	v_add_f32_e32 v5, v5, v6
	v_mov_b32_e32 v6, v5
	s_nop 1
	v_permlane32_swap_b32_e32 v6, v5
	s_and_saveexec_b64 s[8:9], s[0:1]
	s_cbranch_execz .LBB0_1031
	s_waitcnt lgkmcnt(0)
	v_add_f32_e32 v5, v5, v6
	ds_write_b32 v3, v5 offset:512
.LBB0_1031:
	s_or_b64 exec, exec, s[8:9]
	v_mul_f32_e32 v5, v143, v143
	s_waitcnt lgkmcnt(0)
	v_mul_f32_e32 v6, v139, v139
	v_fmac_f32_e32 v5, v142, v142
	v_fmac_f32_e32 v6, v138, v138
	v_fmac_f32_e32 v5, v144, v144
	v_fmac_f32_e32 v6, v140, v140
	v_fmac_f32_e32 v5, v145, v145
	v_fmac_f32_e32 v6, v141, v141
	v_add_f32_e32 v5, v5, v6
	v_mul_f32_e32 v6, v135, v135
	v_fmac_f32_e32 v6, v134, v134
	v_fmac_f32_e32 v6, v136, v136
	v_fmac_f32_e32 v6, v137, v137
	v_add_f32_e32 v5, v5, v6
	v_mul_f32_e32 v6, v131, v131
	v_fmac_f32_e32 v6, v130, v130
	v_fmac_f32_e32 v6, v132, v132
	v_fmac_f32_e32 v6, v133, v133
	v_add_f32_e32 v5, v5, v6
	ds_bpermute_b32 v6, v2, v5
	s_waitcnt lgkmcnt(0)
	v_add_f32_e32 v5, v5, v6
	v_mov_b32_e32 v6, v5
	s_nop 1
	v_permlane32_swap_b32_e32 v6, v5
	s_and_saveexec_b64 s[8:9], s[0:1]
	s_cbranch_execz .LBB0_1033
	s_waitcnt lgkmcnt(0)
	v_add_f32_e32 v5, v5, v6
	ds_write_b32 v3, v5 offset:768
;     __device__ __forceinline__ void operator()(const f32x4 (&acc)[2][2][4][2], const Unit& u, int wr, int wc, int fr, int fq) const {
;     ...
;                 for (int m = 0; m < 4; ++m) { float s_ = 0.f;
; #pragma unroll
;                     for (int q = 0; q < 4; ++q) { const f32x4 v = acc[ai][q >> 1][m][q & 1]; s_ += v[0] * v[0] + v[1] * v[1] + v[2] * v[2] + v[3] * v[3]; }
;                     s_ += __shfl_xor(s_, 16); s_ += __shfl_xor(s_, 32);
;                     if (fq == 0) xb[(ai * HALF + m * 16) * 4 + wc] = s_; }
.LBB0_1033:
	s_or_b64 exec, exec, s[8:9]
	v_mul_f32_e32 v5, v127, v127
	s_waitcnt lgkmcnt(0)
	v_mul_f32_e32 v6, v123, v123
	v_fmac_f32_e32 v5, v126, v126
	v_fmac_f32_e32 v6, v122, v122
	v_fmac_f32_e32 v5, v128, v128
	v_fmac_f32_e32 v6, v124, v124
	v_fmac_f32_e32 v5, v129, v129
	v_fmac_f32_e32 v6, v125, v125
	v_add_f32_e32 v5, v5, v6
	v_mul_f32_e32 v6, v119, v119
	v_fmac_f32_e32 v6, v118, v118
	v_fmac_f32_e32 v6, v120, v120
	v_fmac_f32_e32 v6, v121, v121
	v_add_f32_e32 v5, v5, v6
	v_mul_f32_e32 v6, v115, v115
	v_fmac_f32_e32 v6, v114, v114
	v_fmac_f32_e32 v6, v116, v116
	v_fmac_f32_e32 v6, v117, v117
	v_add_f32_e32 v5, v5, v6
	ds_bpermute_b32 v6, v2, v5
	s_waitcnt lgkmcnt(0)
	v_add_f32_e32 v5, v5, v6
	v_mov_b32_e32 v6, v5
	s_nop 1
	v_permlane32_swap_b32_e32 v6, v5
	s_and_saveexec_b64 s[8:9], s[0:1]
	s_cbranch_execz .LBB0_1035
	s_waitcnt lgkmcnt(0)
	v_add_f32_e32 v5, v5, v6
	ds_write_b32 v3, v5 offset:2048
.LBB0_1035:
	s_or_b64 exec, exec, s[8:9]
	v_mul_f32_e32 v5, v111, v111
	s_waitcnt lgkmcnt(0)
	v_mul_f32_e32 v6, v107, v107
	v_fmac_f32_e32 v5, v110, v110
	v_fmac_f32_e32 v6, v106, v106
	v_fmac_f32_e32 v5, v112, v112
	v_fmac_f32_e32 v6, v108, v108
	v_fmac_f32_e32 v5, v113, v113
	v_fmac_f32_e32 v6, v109, v109
	v_add_f32_e32 v5, v5, v6
	v_mul_f32_e32 v6, v103, v103
	v_fmac_f32_e32 v6, v102, v102
	v_fmac_f32_e32 v6, v104, v104
	v_fmac_f32_e32 v6, v105, v105
	v_add_f32_e32 v5, v5, v6
	v_mul_f32_e32 v6, v99, v99
	v_fmac_f32_e32 v6, v98, v98
	v_fmac_f32_e32 v6, v100, v100
	v_fmac_f32_e32 v6, v101, v101
	v_add_f32_e32 v5, v5, v6
	ds_bpermute_b32 v6, v2, v5
	s_waitcnt lgkmcnt(0)
	v_add_f32_e32 v5, v5, v6
	v_mov_b32_e32 v6, v5
	s_nop 1
	v_permlane32_swap_b32_e32 v6, v5
	s_and_saveexec_b64 s[8:9], s[0:1]
	s_cbranch_execz .LBB0_1037
	s_waitcnt lgkmcnt(0)
	v_add_f32_e32 v5, v5, v6
	ds_write_b32 v3, v5 offset:2304
.LBB0_1037:
	s_or_b64 exec, exec, s[8:9]
	v_mul_f32_e32 v5, v95, v95
	s_waitcnt lgkmcnt(0)
	v_mul_f32_e32 v6, v91, v91
	v_fmac_f32_e32 v5, v94, v94
	v_fmac_f32_e32 v6, v90, v90
	v_fmac_f32_e32 v5, v96, v96
	v_fmac_f32_e32 v6, v92, v92
	v_fmac_f32_e32 v5, v97, v97
	v_fmac_f32_e32 v6, v93, v93
	v_add_f32_e32 v5, v5, v6
	v_mul_f32_e32 v6, v87, v87
	v_fmac_f32_e32 v6, v86, v86
	v_fmac_f32_e32 v6, v88, v88
	v_fmac_f32_e32 v6, v89, v89
	v_add_f32_e32 v5, v5, v6
	v_mul_f32_e32 v6, v83, v83
	v_fmac_f32_e32 v6, v82, v82
	v_fmac_f32_e32 v6, v84, v84
	v_fmac_f32_e32 v6, v85, v85
	v_add_f32_e32 v5, v5, v6
	ds_bpermute_b32 v6, v2, v5
	s_waitcnt lgkmcnt(0)
	v_add_f32_e32 v5, v5, v6
	v_mov_b32_e32 v6, v5
	s_nop 1
	v_permlane32_swap_b32_e32 v6, v5
	s_and_saveexec_b64 s[8:9], s[0:1]
	s_cbranch_execz .LBB0_1039
	s_waitcnt lgkmcnt(0)
	v_add_f32_e32 v5, v5, v6
	ds_write_b32 v3, v5 offset:2560
.LBB0_1039:
	s_or_b64 exec, exec, s[8:9]
	v_mul_f32_e32 v5, v79, v79
	s_waitcnt lgkmcnt(0)
	v_mul_f32_e32 v6, v75, v75
	v_fmac_f32_e32 v5, v78, v78
	v_fmac_f32_e32 v6, v74, v74
	v_fmac_f32_e32 v5, v80, v80
	v_fmac_f32_e32 v6, v76, v76
	v_fmac_f32_e32 v5, v81, v81
	v_fmac_f32_e32 v6, v77, v77
	v_add_f32_e32 v5, v5, v6
	v_mul_f32_e32 v6, v71, v71
	v_fmac_f32_e32 v6, v70, v70
	v_fmac_f32_e32 v6, v72, v72
	v_fmac_f32_e32 v6, v73, v73
	v_add_f32_e32 v5, v5, v6
	v_mul_f32_e32 v6, v67, v67
	v_fmac_f32_e32 v6, v66, v66
	v_fmac_f32_e32 v6, v68, v68
	v_fmac_f32_e32 v6, v69, v69
	v_add_f32_e32 v5, v5, v6
	ds_bpermute_b32 v2, v2, v5
	s_waitcnt lgkmcnt(0)
	v_add_f32_e32 v2, v5, v2
	v_mov_b32_e32 v4, v2
	s_nop 1
	v_permlane32_swap_b32_e32 v4, v2
	s_and_saveexec_b64 s[8:9], s[0:1]
	s_cbranch_execz .LBB0_1041
	s_waitcnt lgkmcnt(0)
	v_add_f32_e32 v2, v2, v4
	ds_write_b32 v3, v2 offset:2816
